# speedup vs baseline: 1.0113x; 1.0113x over previous
.LBB2_45:
	s_waitcnt lgkmcnt(1)
	ds_read_b32 v4, v134
	s_waitcnt lgkmcnt(0)
	v_ashrrev_i32_e32 v2, 6, v4
	v_and_b32_e32 v3, 63, v4
	v_add_u32_e32 v152, v2, v129
	v_add_u32_e32 v153, v3, v130
	v_max_u32_e32 v154, v152, v153
	v_mov_b64_e32 v[156:157], 0
	v_cmp_gt_u32_e64 s[98:99], 64, v154
	v_lshlrev_b32_e32 v154, 6, v152
	v_or3_b32 v154, v154, s78, v153
	v_mov_b32_e32 v155, 0
	s_and_b64 s[98:99], s[98:99], s[58:59]
	v_lshl_add_u64 v[154:155], v[154:155], 3, s[82:83]
	s_and_saveexec_b64 s[96:97], s[98:99]
	global_load_dwordx2 v[156:157], v[154:155], off
	s_or_b64 exec, exec, s[96:97]
	v_add_u32_e32 v10, -1, v2
	v_add_u32_e32 v14, -1, v3
	v_lshlrev_b32_e32 v11, 6, v10
	v_and_b32_e32 v17, 0xffffffc0, v4
	v_or_b32_e32 v8, v10, v14
	v_add_u32_e32 v6, v11, v14
	v_add_u32_e32 v15, 1, v3
	v_add_u32_e32 v12, v14, v17
	v_ashrrev_i32_e32 v7, 31, v6
	v_cmp_gt_u32_e64 s[20:21], 64, v8
	v_or_b32_e32 v8, v11, v3
	v_cmp_gt_u32_e64 s[14:15], 64, v10
	v_add_u32_e32 v10, v11, v15
	v_or_b32_e32 v16, v14, v2
	v_ashrrev_i32_e32 v13, 31, v12
	v_lshlrev_b64 v[6:7], 7, v[6:7]
	v_ashrrev_i32_e32 v9, 31, v8
	v_cmp_ne_u32_e32 vcc, 63, v3
	v_ashrrev_i32_e32 v11, 31, v10
	v_lshlrev_b64 v[12:13], 7, v[12:13]
	v_cmp_gt_u32_e64 s[12:13], 64, v16
	v_cndmask_b32_e64 v7, 0, v7, s[20:21]
	v_cndmask_b32_e64 v6, 0, v6, s[20:21]
	v_lshlrev_b64 v[8:9], 7, v[8:9]
	v_lshlrev_b64 v[10:11], 7, v[10:11]
	s_and_b64 s[10:11], vcc, s[14:15]
	v_cndmask_b32_e64 v13, 0, v13, s[12:13]
	v_cndmask_b32_e64 v12, 0, v12, s[12:13]
	v_lshl_add_u64 v[6:7], v[6:7], 2, v[56:57]
	v_cndmask_b32_e64 v9, 0, v9, s[14:15]
	v_cndmask_b32_e64 v8, 0, v8, s[14:15]
	v_cndmask_b32_e64 v11, 0, v11, s[10:11]
	v_cndmask_b32_e64 v10, 0, v10, s[10:11]
	v_lshl_add_u64 v[12:13], v[12:13], 2, v[56:57]
	v_lshl_add_u64 v[8:9], v[8:9], 2, v[56:57]
	v_lshl_add_u64 v[10:11], v[10:11], 2, v[56:57]
	global_load_dwordx2 v[72:73], v[6:7], off
	global_load_dwordx2 v[68:69], v[8:9], off
	global_load_dwordx2 v[64:65], v[10:11], off
	global_load_dwordx2 v[60:61], v[12:13], off
	v_add_u32_e32 v12, 1, v2
	v_or_b32_e32 v10, v12, v14
	v_lshlrev_b32_e32 v13, 6, v12
	v_cmp_gt_u32_e64 s[18:19], 64, v10
	v_or_b32_e32 v10, v13, v3
	v_ashrrev_i32_e32 v5, 31, v4
	v_add_u32_e32 v6, v15, v17
	v_add_u32_e32 v8, v13, v14
	v_ashrrev_i32_e32 v11, 31, v10
	v_lshlrev_b64 v[4:5], 7, v[4:5]
	v_cmp_gt_u32_e64 s[40:41], 64, v2
	v_ashrrev_i32_e32 v7, 31, v6
	v_ashrrev_i32_e32 v9, 31, v8
	v_lshlrev_b64 v[10:11], 7, v[10:11]
	v_cmp_gt_u32_e64 s[8:9], 64, v12
	v_cndmask_b32_e64 v5, 0, v5, s[40:41]
	v_cndmask_b32_e64 v4, 0, v4, s[40:41]
	v_lshlrev_b64 v[6:7], 7, v[6:7]
	s_and_b64 s[16:17], s[40:41], vcc
	v_lshlrev_b64 v[8:9], 7, v[8:9]
	v_cndmask_b32_e64 v11, 0, v11, s[8:9]
	v_cndmask_b32_e64 v10, 0, v10, s[8:9]
	v_lshl_add_u64 v[4:5], v[4:5], 2, v[56:57]
	v_cndmask_b32_e64 v7, 0, v7, s[16:17]
	v_cndmask_b32_e64 v6, 0, v6, s[16:17]
	v_cndmask_b32_e64 v9, 0, v9, s[18:19]
	v_cndmask_b32_e64 v8, 0, v8, s[18:19]
	v_lshl_add_u64 v[10:11], v[10:11], 2, v[56:57]
	v_lshl_add_u64 v[6:7], v[6:7], 2, v[56:57]
	v_lshl_add_u64 v[8:9], v[8:9], 2, v[56:57]
	global_load_dwordx2 v[90:91], v[4:5], off
	global_load_dwordx2 v[66:67], v[6:7], off
	global_load_dwordx2 v[62:63], v[8:9], off
	global_load_dwordx2 v[58:59], v[10:11], off
	v_add_u32_e32 v10, -2, v2
	v_add_u32_e32 v4, v13, v15
	v_add_u32_e32 v12, -2, v3
	v_lshlrev_b32_e32 v11, 6, v10
	v_add_u32_e32 v13, 2, v3
	v_or_b32_e32 v8, v10, v12
	v_cmp_gt_u32_e64 s[34:35], 64, v10
	v_add_u32_e32 v10, v11, v13
	v_ashrrev_i32_e32 v5, 31, v4
	s_and_b64 s[6:7], vcc, s[8:9]
	v_add_u32_e32 v6, v11, v12
	v_cmp_gt_u32_e64 s[38:39], 64, v8
	v_or_b32_e32 v8, v11, v3
	v_cmp_gt_u32_e32 vcc, 62, v3
	v_ashrrev_i32_e32 v11, 31, v10
	v_lshlrev_b64 v[4:5], 7, v[4:5]
	v_ashrrev_i32_e32 v7, 31, v6
	v_ashrrev_i32_e32 v9, 31, v8
	v_lshlrev_b64 v[10:11], 7, v[10:11]
	s_and_b64 s[30:31], vcc, s[34:35]
	v_cndmask_b32_e64 v5, 0, v5, s[6:7]
	v_cndmask_b32_e64 v4, 0, v4, s[6:7]
	v_lshlrev_b64 v[6:7], 7, v[6:7]
	v_lshlrev_b64 v[8:9], 7, v[8:9]
	v_cndmask_b32_e64 v11, 0, v11, s[30:31]
	v_cndmask_b32_e64 v10, 0, v10, s[30:31]
	v_lshl_add_u64 v[4:5], v[4:5], 2, v[56:57]
	v_cndmask_b32_e64 v7, 0, v7, s[38:39]
	v_cndmask_b32_e64 v6, 0, v6, s[38:39]
	v_cndmask_b32_e64 v9, 0, v9, s[34:35]
	v_cndmask_b32_e64 v8, 0, v8, s[34:35]
	v_lshl_add_u64 v[10:11], v[10:11], 2, v[56:57]
	v_add_u32_e32 v14, 2, v2
	v_lshl_add_u64 v[6:7], v[6:7], 2, v[56:57]
	v_lshl_add_u64 v[8:9], v[8:9], 2, v[56:57]
	global_load_dwordx2 v[70:71], v[4:5], off
	global_load_dwordx2 v[84:85], v[6:7], off
	global_load_dwordx2 v[80:81], v[8:9], off
	global_load_dwordx2 v[76:77], v[10:11], off
	v_or_b32_e32 v10, v14, v12
	v_lshlrev_b32_e32 v15, 6, v14
	v_or_b32_e32 v6, v12, v2
	v_add_u32_e32 v4, v12, v17
	v_cmp_gt_u32_e64 s[28:29], 64, v10
	v_or_b32_e32 v10, v15, v3
	v_ashrrev_i32_e32 v5, 31, v4
	v_cmp_gt_u32_e64 s[36:37], 64, v6
	v_add_u32_e32 v6, v13, v17
	v_add_u32_e32 v8, v15, v12
	v_ashrrev_i32_e32 v11, 31, v10
	v_lshlrev_b64 v[4:5], 7, v[4:5]
	v_ashrrev_i32_e32 v7, 31, v6
	v_ashrrev_i32_e32 v9, 31, v8
	v_lshlrev_b64 v[10:11], 7, v[10:11]
	v_cmp_gt_u32_e64 s[22:23], 64, v14
	v_cndmask_b32_e64 v5, 0, v5, s[36:37]
	v_cndmask_b32_e64 v4, 0, v4, s[36:37]
	v_lshlrev_b64 v[6:7], 7, v[6:7]
	s_and_b64 s[26:27], s[40:41], vcc
	v_lshlrev_b64 v[8:9], 7, v[8:9]
	v_cndmask_b32_e64 v11, 0, v11, s[22:23]
	v_cndmask_b32_e64 v10, 0, v10, s[22:23]
	v_lshl_add_u64 v[4:5], v[4:5], 2, v[56:57]
	v_cndmask_b32_e64 v7, 0, v7, s[26:27]
	v_cndmask_b32_e64 v6, 0, v6, s[26:27]
	v_cndmask_b32_e64 v9, 0, v9, s[28:29]
	v_cndmask_b32_e64 v8, 0, v8, s[28:29]
	v_lshl_add_u64 v[10:11], v[10:11], 2, v[56:57]
	v_lshl_add_u64 v[6:7], v[6:7], 2, v[56:57]
	v_lshl_add_u64 v[8:9], v[8:9], 2, v[56:57]
	global_load_dwordx2 v[88:89], v[4:5], off
	global_load_dwordx2 v[82:83], v[6:7], off
	global_load_dwordx2 v[78:79], v[8:9], off
	global_load_dwordx2 v[74:75], v[10:11], off
	v_add_u32_e32 v10, -3, v2
	v_add_u32_e32 v4, v15, v13
	v_add_u32_e32 v12, -3, v3
	v_lshlrev_b32_e32 v11, 6, v10
	v_add_u32_e32 v13, 3, v3
	v_or_b32_e32 v8, v10, v12
	v_add_u32_e32 v6, v11, v12
	v_cmp_gt_u32_e64 s[52:53], 64, v10
	v_add_u32_e32 v10, v11, v13
	v_ashrrev_i32_e32 v5, 31, v4
	s_and_b64 s[24:25], vcc, s[22:23]
	v_ashrrev_i32_e32 v7, 31, v6
	v_cmp_gt_u32_e64 s[56:57], 64, v8
	v_or_b32_e32 v8, v11, v3
	v_cmp_gt_u32_e32 vcc, 61, v3
	v_ashrrev_i32_e32 v11, 31, v10
	v_lshlrev_b64 v[4:5], 7, v[4:5]
	v_lshlrev_b64 v[6:7], 7, v[6:7]
	v_ashrrev_i32_e32 v9, 31, v8
	v_lshlrev_b64 v[10:11], 7, v[10:11]
	s_and_b64 s[50:51], vcc, s[52:53]
	v_cndmask_b32_e64 v5, 0, v5, s[24:25]
	v_cndmask_b32_e64 v4, 0, v4, s[24:25]
	v_cndmask_b32_e64 v7, 0, v7, s[56:57]
	v_cndmask_b32_e64 v6, 0, v6, s[56:57]
	v_lshlrev_b64 v[8:9], 7, v[8:9]
	v_cndmask_b32_e64 v11, 0, v11, s[50:51]
	v_cndmask_b32_e64 v10, 0, v10, s[50:51]
	v_lshl_add_u64 v[4:5], v[4:5], 2, v[56:57]
	v_lshl_add_u64 v[6:7], v[6:7], 2, v[56:57]
	v_cndmask_b32_e64 v9, 0, v9, s[52:53]
	v_cndmask_b32_e64 v8, 0, v8, s[52:53]
	v_lshl_add_u64 v[10:11], v[10:11], 2, v[56:57]
	v_add_u32_e32 v14, 3, v2
	v_lshl_add_u64 v[8:9], v[8:9], 2, v[56:57]
	global_load_dwordx2 v[86:87], v[4:5], off
	global_load_dwordx2 v[106:107], v[6:7], off
	global_load_dwordx2 v[104:105], v[8:9], off
	global_load_dwordx2 v[100:101], v[10:11], off
	v_or_b32_e32 v6, v12, v2
	v_add_u32_e32 v4, v12, v17
	v_or_b32_e32 v10, v14, v12
	v_lshlrev_b32_e32 v15, 6, v14
	v_ashrrev_i32_e32 v5, 31, v4
	v_cmp_gt_u32_e64 s[54:55], 64, v6
	v_add_u32_e32 v6, v13, v17
	v_add_u32_e32 v8, v15, v12
	v_cmp_gt_u32_e64 s[48:49], 64, v10
	v_or_b32_e32 v10, v15, v3
	v_lshlrev_b64 v[4:5], 7, v[4:5]
	v_ashrrev_i32_e32 v7, 31, v6
	v_ashrrev_i32_e32 v9, 31, v8
	v_ashrrev_i32_e32 v11, 31, v10
	v_cndmask_b32_e64 v5, 0, v5, s[54:55]
	v_cndmask_b32_e64 v4, 0, v4, s[54:55]
	v_lshlrev_b64 v[6:7], 7, v[6:7]
	s_and_b64 s[46:47], s[40:41], vcc
	v_lshlrev_b64 v[8:9], 7, v[8:9]
	v_lshlrev_b64 v[10:11], 7, v[10:11]
	v_cmp_gt_u32_e64 s[0:1], 64, v14
	v_lshl_add_u64 v[4:5], v[4:5], 2, v[56:57]
	v_cndmask_b32_e64 v7, 0, v7, s[46:47]
	v_cndmask_b32_e64 v6, 0, v6, s[46:47]
	v_cndmask_b32_e64 v9, 0, v9, s[48:49]
	v_cndmask_b32_e64 v8, 0, v8, s[48:49]
	v_cndmask_b32_e64 v11, 0, v11, s[0:1]
	v_cndmask_b32_e64 v10, 0, v10, s[0:1]
	v_lshl_add_u64 v[6:7], v[6:7], 2, v[56:57]
	v_lshl_add_u64 v[8:9], v[8:9], 2, v[56:57]
	v_lshl_add_u64 v[10:11], v[10:11], 2, v[56:57]
	global_load_dwordx2 v[108:109], v[4:5], off
	global_load_dwordx2 v[102:103], v[6:7], off
	global_load_dwordx2 v[98:99], v[8:9], off
	global_load_dwordx2 v[96:97], v[10:11], off
	v_add_u32_e32 v4, v15, v13
	v_ashrrev_i32_e32 v5, 31, v4
	v_lshlrev_b64 v[4:5], 7, v[4:5]
	s_and_b64 s[44:45], vcc, s[0:1]
	v_cndmask_b32_e64 v5, 0, v5, s[44:45]
	v_cndmask_b32_e64 v4, 0, v4, s[44:45]
	v_lshl_add_u64 v[4:5], v[4:5], 2, v[56:57]
	global_load_dwordx2 v[94:95], v[4:5], off
	s_and_saveexec_b64 s[96:97], s[58:59]
	s_cbranch_execz .LBB2_49
	s_waitcnt vmcnt(27)
	ds_write_b64 v131, v[156:157] offset:62976
